# DeltaNet scan: static s_setprio 3 on the two compute waves for the duration of the scan
# speedup vs baseline: 1.0020x; 1.0020x over previous
.LBB0_765:
	s_setprio 3
	s_cmp_gt_u32 s68, 3
	s_mov_b64 s[8:9], -1
	s_cbranch_scc0 .LBB0_767
	s_add_i32 s10, s46, 1
	s_and_b64 s[8:9], s[72:73], exec
	s_cselect_b32 s8, s47, s10
	s_add_i32 s10, s8, s71
	s_mov_b64 s[8:9], 0

.LBB0_773:
	s_setprio 0
	v_readlane_b32 s64, v255, 8
	v_readlane_b32 s72, v255, 17
	v_readlane_b32 s86, v255, 19
	v_readlane_b32 s94, v255, 21
	v_readlane_b32 s96, v255, 23
	v_readlane_b32 s60, v255, 25
	v_readlane_b32 s58, v255, 6
	s_waitcnt lgkmcnt(0)
	s_barrier
	v_readlane_b32 s65, v255, 9
	v_readlane_b32 s66, v255, 10
	v_readlane_b32 s67, v255, 11
	v_readlane_b32 s68, v255, 12
	v_readlane_b32 s69, v255, 13
	v_readlane_b32 s70, v255, 14
	v_readlane_b32 s71, v255, 15
	v_readlane_b32 s74, v255, 16
	v_readlane_b32 s73, v255, 18
	v_readlane_b32 s87, v255, 20
	v_readlane_b32 s95, v255, 22
	v_readlane_b32 s97, v255, 24
	v_readlane_b32 s61, v255, 26
	s_movk_i32 s54, 0x1000
	v_readlane_b32 s59, v255, 7
